# saddr-form LDS-DMA also in MLP1 K-loop (scalar bases incl. the +hstepB variant formed once per iteration)
# speedup vs baseline: 1.0159x; 1.0028x over previous
.LBB5_53:
	v_mov_b32_e32 v95, 0
	s_andn2_b64 vcc, exec, s[24:25]
	v_mov_b32_e32 v94, v95
	v_mov_b32_e32 v93, v95
	v_mov_b32_e32 v92, v95
	v_mov_b32_e32 v91, v95
	v_mov_b32_e32 v90, v95
	v_mov_b32_e32 v89, v95
	v_mov_b32_e32 v88, v95
	v_mov_b32_e32 v79, v95
	v_mov_b32_e32 v78, v95
	v_mov_b32_e32 v77, v95
	v_mov_b32_e32 v76, v95
	v_mov_b32_e32 v75, v95
	v_mov_b32_e32 v74, v95
	v_mov_b32_e32 v73, v95
	v_mov_b32_e32 v72, v95
	v_mov_b32_e32 v31, v95
	v_mov_b32_e32 v30, v95
	v_mov_b32_e32 v29, v95
	v_mov_b32_e32 v28, v95
	v_mov_b32_e32 v27, v95
	v_mov_b32_e32 v26, v95
	v_mov_b32_e32 v25, v95
	v_mov_b32_e32 v24, v95
	v_mov_b32_e32 v15, v95
	v_mov_b32_e32 v14, v95
	v_mov_b32_e32 v13, v95
	v_mov_b32_e32 v12, v95
	v_mov_b32_e32 v11, v95
	v_mov_b32_e32 v10, v95
	v_mov_b32_e32 v9, v95
	v_mov_b32_e32 v8, v95
	v_mov_b32_e32 v87, v95
	v_mov_b32_e32 v86, v95
	v_mov_b32_e32 v85, v95
	v_mov_b32_e32 v84, v95
	v_mov_b32_e32 v83, v95
	v_mov_b32_e32 v82, v95
	v_mov_b32_e32 v81, v95
	v_mov_b32_e32 v80, v95
	v_mov_b32_e32 v55, v95
	v_mov_b32_e32 v54, v95
	v_mov_b32_e32 v53, v95
	v_mov_b32_e32 v52, v95
	v_mov_b32_e32 v51, v95
	v_mov_b32_e32 v50, v95
	v_mov_b32_e32 v49, v95
	v_mov_b32_e32 v48, v95
	v_mov_b32_e32 v23, v95
	v_mov_b32_e32 v22, v95
	v_mov_b32_e32 v21, v95
	v_mov_b32_e32 v20, v95
	v_mov_b32_e32 v19, v95
	v_mov_b32_e32 v18, v95
	v_mov_b32_e32 v17, v95
	v_mov_b32_e32 v16, v95
	v_mov_b32_e32 v7, v95
	v_mov_b32_e32 v6, v95
	v_mov_b32_e32 v5, v95
	v_mov_b32_e32 v4, v95
	v_mov_b32_e32 v3, v95
	v_mov_b32_e32 v2, v95
	v_mov_b32_e32 v1, v95
	v_mov_b32_e32 v0, v95
	s_cbranch_vccnz .LBB5_42
	v_mov_b32_e32 v0, 0
	v_lshl_add_u64 v[32:33], s[40:41], 0, v[112:113]
	v_lshl_add_u64 v[34:35], s[40:41], 0, v[114:115]
	v_lshl_add_u64 v[36:37], s[42:43], 0, v[116:117]
	v_lshl_add_u64 v[38:39], s[42:43], 0, v[118:119]
	v_lshl_add_u64 v[40:41], s[42:43], 0, v[120:121]
	v_lshl_add_u64 v[42:43], s[42:43], 0, v[122:123]
	s_mov_b32 s75, 0
	s_mov_b64 s[44:45], 0
	v_mov_b32_e32 v1, v0
	v_mov_b32_e32 v2, v0
	v_mov_b32_e32 v3, v0
	v_mov_b32_e32 v4, v0
	v_mov_b32_e32 v5, v0
	v_mov_b32_e32 v6, v0
	v_mov_b32_e32 v7, v0
	v_mov_b32_e32 v16, v0
	v_mov_b32_e32 v17, v0
	v_mov_b32_e32 v18, v0
	v_mov_b32_e32 v19, v0
	v_mov_b32_e32 v20, v0
	v_mov_b32_e32 v21, v0
	v_mov_b32_e32 v22, v0
	v_mov_b32_e32 v23, v0
	v_mov_b32_e32 v48, v0
	v_mov_b32_e32 v49, v0
	v_mov_b32_e32 v50, v0
	v_mov_b32_e32 v51, v0
	v_mov_b32_e32 v52, v0
	v_mov_b32_e32 v53, v0
	v_mov_b32_e32 v54, v0
	v_mov_b32_e32 v55, v0
	v_mov_b32_e32 v80, v0
	v_mov_b32_e32 v81, v0
	v_mov_b32_e32 v82, v0
	v_mov_b32_e32 v83, v0
	v_mov_b32_e32 v84, v0
	v_mov_b32_e32 v85, v0
	v_mov_b32_e32 v86, v0
	v_mov_b32_e32 v87, v0
	v_mov_b32_e32 v8, v0
	v_mov_b32_e32 v9, v0
	v_mov_b32_e32 v10, v0
	v_mov_b32_e32 v11, v0
	v_mov_b32_e32 v12, v0
	v_mov_b32_e32 v13, v0
	v_mov_b32_e32 v14, v0
	v_mov_b32_e32 v15, v0
	v_mov_b32_e32 v24, v0
	v_mov_b32_e32 v25, v0
	v_mov_b32_e32 v26, v0
	v_mov_b32_e32 v27, v0
	v_mov_b32_e32 v28, v0
	v_mov_b32_e32 v29, v0
	v_mov_b32_e32 v30, v0
	v_mov_b32_e32 v31, v0
	v_mov_b32_e32 v72, v0
	v_mov_b32_e32 v73, v0
	v_mov_b32_e32 v74, v0
	v_mov_b32_e32 v75, v0
	v_mov_b32_e32 v76, v0
	v_mov_b32_e32 v77, v0
	v_mov_b32_e32 v78, v0
	v_mov_b32_e32 v79, v0
	v_mov_b32_e32 v88, v0
	v_mov_b32_e32 v89, v0
	v_mov_b32_e32 v90, v0
	v_mov_b32_e32 v91, v0
	v_mov_b32_e32 v92, v0
	v_mov_b32_e32 v93, v0
	v_mov_b32_e32 v94, v0
	v_mov_b32_e32 v95, v0
	s_add_u32 s78, s40, s44
	s_addc_u32 s79, s41, s45
	s_add_u32 s80, s42, s44
	s_addc_u32 s81, s43, s45
	s_add_u32 s46, s40, s44
	s_addc_u32 s47, s41, s45
	s_add_u32 s46, s46, 0x180
	s_addc_u32 s47, s47, 0
	s_add_u32 s48, s42, s44
	s_addc_u32 s49, s43, s45
	s_add_u32 s76, s48, 0x180
	s_addc_u32 s77, s49, 0
	s_cmp_eq_u32 s67, s75
	s_cselect_b32 s49, s7, s47
	s_cselect_b32 s48, s6, s46
	s_cselect_b32 s47, s5, s77
	s_cselect_b32 s46, s4, s76
	s_add_u32 s82, s48, 0x80
	s_addc_u32 s83, s49, 0
	s_add_u32 s84, s46, 0x80
	s_addc_u32 s85, s47, 0
	s_add_u32 s86, s84, s10
	s_addc_u32 s87, s85, s11
	s_add_i32 s76, s19, s54
.LBB5_55:
	s_mov_b32 m0, s76
	ds_read_b128 v[44:47], v130 offset:16384
	ds_read_b128 v[56:59], v130 offset:17408
	ds_read_b128 v[60:63], v130 offset:18432
	ds_read_b128 v[64:67], v130 offset:19456
	ds_read_b128 v[68:71], v131
	ds_read_b128 v[96:99], v131 offset:1024
	ds_read_b128 v[136:139], v131 offset:2048
	ds_read_b128 v[140:143], v131 offset:3072
	ds_read_b128 v[144:147], v131 offset:4096
	ds_read_b128 v[148:151], v131 offset:5120
	ds_read_b128 v[152:155], v131 offset:6144
	ds_read_b128 v[156:159], v131 offset:7168
	global_load_lds_dwordx4 v112, s[78:79]
	s_add_i32 m0, s76, 0x2000
	s_add_i32 s76, s27, s54
	global_load_lds_dwordx4 v114, s[78:79]
	s_mov_b32 m0, s76
	s_nop 0
	global_load_lds_dwordx4 v116, s[80:81]
	s_add_i32 m0, s76, 0x2000
	s_nop 0
	global_load_lds_dwordx4 v118, s[80:81]
	s_barrier
	s_setprio 1
	s_waitcnt lgkmcnt(7)
	v_mfma_f32_16x16x32_f16 v[92:95], v[44:47], v[68:71], v[92:95]
	v_mfma_f32_16x16x32_f16 v[88:91], v[60:63], v[68:71], v[88:91]
	s_waitcnt lgkmcnt(5)
	v_mfma_f32_16x16x32_f16 v[76:79], v[44:47], v[136:139], v[76:79]
	v_mfma_f32_16x16x32_f16 v[72:75], v[60:63], v[136:139], v[72:75]
	s_waitcnt lgkmcnt(3)
	v_mfma_f32_16x16x32_f16 v[28:31], v[44:47], v[144:147], v[28:31]
	v_mfma_f32_16x16x32_f16 v[24:27], v[60:63], v[144:147], v[24:27]
	s_waitcnt lgkmcnt(1)
	v_mfma_f32_16x16x32_f16 v[12:15], v[44:47], v[152:155], v[12:15]
	v_mfma_f32_16x16x32_f16 v[8:11], v[60:63], v[152:155], v[8:11]
	v_mfma_f32_16x16x32_f16 v[92:95], v[56:59], v[96:99], v[92:95]
	v_mfma_f32_16x16x32_f16 v[88:91], v[64:67], v[96:99], v[88:91]
	v_mfma_f32_16x16x32_f16 v[76:79], v[56:59], v[140:143], v[76:79]
	v_mfma_f32_16x16x32_f16 v[72:75], v[64:67], v[140:143], v[72:75]
	v_mfma_f32_16x16x32_f16 v[28:31], v[56:59], v[148:151], v[28:31]
	v_mfma_f32_16x16x32_f16 v[24:27], v[64:67], v[148:151], v[24:27]
	s_waitcnt lgkmcnt(0)
	v_mfma_f32_16x16x32_f16 v[12:15], v[56:59], v[156:159], v[12:15]
	v_mfma_f32_16x16x32_f16 v[8:11], v[64:67], v[156:159], v[8:11]
	s_setprio 0
	s_barrier
	s_add_i32 s76, s68, s54
	s_mov_b32 m0, s76
	ds_read_b128 v[44:47], v130 offset:32768
	ds_read_b128 v[56:59], v130 offset:33792
	ds_read_b128 v[60:63], v130 offset:34816
	ds_read_b128 v[64:67], v130 offset:35840
	global_load_lds_dwordx4 v120, s[80:81]
	s_add_i32 m0, s76, 0x2000
	s_nop 0
	global_load_lds_dwordx4 v122, s[80:81]
	s_waitcnt vmcnt(6)
	s_barrier
	s_setprio 1
	s_waitcnt lgkmcnt(3)
	v_mfma_f32_16x16x32_f16 v[84:87], v[44:47], v[68:71], v[84:87]
	v_mfma_f32_16x16x32_f16 v[52:55], v[44:47], v[136:139], v[52:55]
	s_waitcnt lgkmcnt(1)
	v_mfma_f32_16x16x32_f16 v[48:51], v[60:63], v[136:139], v[48:51]
	v_mfma_f32_16x16x32_f16 v[20:23], v[44:47], v[144:147], v[20:23]
	v_mfma_f32_16x16x32_f16 v[16:19], v[60:63], v[144:147], v[16:19]
	v_mfma_f32_16x16x32_f16 v[4:7], v[44:47], v[152:155], v[4:7]
	v_mfma_f32_16x16x32_f16 v[0:3], v[60:63], v[152:155], v[0:3]
	v_mfma_f32_16x16x32_f16 v[84:87], v[56:59], v[96:99], v[84:87]
	v_mfma_f32_16x16x32_f16 v[68:71], v[60:63], v[68:71], v[80:83]
	v_mfma_f32_16x16x32_f16 v[52:55], v[56:59], v[140:143], v[52:55]
	s_waitcnt lgkmcnt(0)
	v_mfma_f32_16x16x32_f16 v[48:51], v[64:67], v[140:143], v[48:51]
	v_mfma_f32_16x16x32_f16 v[20:23], v[56:59], v[148:151], v[20:23]
	v_mfma_f32_16x16x32_f16 v[16:19], v[64:67], v[148:151], v[16:19]
	v_mfma_f32_16x16x32_f16 v[4:7], v[56:59], v[156:159], v[4:7]
	v_mfma_f32_16x16x32_f16 v[0:3], v[64:67], v[156:159], v[0:3]
	v_mfma_f32_16x16x32_f16 v[68:71], v[64:67], v[96:99], v[68:71]
	s_setprio 0
	s_barrier
	s_add_i32 s76, 0, 0x10000
	s_mov_b32 m0, s57
	v_add_u32_e32 v64, s76, v128
	ds_read_b128 v[44:47], v64
	ds_read_b128 v[56:59], v64 offset:1024
	ds_read_b128 v[60:63], v64 offset:2048
	ds_read_b128 v[64:67], v64 offset:3072
	ds_read_b128 v[80:83], v131 offset:49152
	ds_read_b128 v[96:99], v131 offset:50176
	ds_read_b128 v[136:139], v131 offset:51200
	ds_read_b128 v[140:143], v131 offset:52224
	ds_read_b128 v[144:147], v131 offset:53248
	ds_read_b128 v[148:151], v131 offset:54272
	ds_read_b128 v[152:155], v131 offset:55296
	ds_read_b128 v[156:159], v131 offset:56320
	global_load_lds_dwordx4 v100, s[48:49]
	s_mov_b32 m0, s58
	s_nop 0
	global_load_lds_dwordx4 v104, s[48:49]
	s_mov_b32 m0, s59
	s_nop 0
	global_load_lds_dwordx4 v102, s[46:47]
	s_mov_b32 m0, s60
	s_nop 0
	global_load_lds_dwordx4 v106, s[46:47]
	s_barrier
	s_setprio 1
	s_waitcnt lgkmcnt(7)
	v_mfma_f32_16x16x32_f16 v[92:95], v[44:47], v[80:83], v[92:95]
	v_mfma_f32_16x16x32_f16 v[88:91], v[60:63], v[80:83], v[88:91]
	s_waitcnt lgkmcnt(5)
	v_mfma_f32_16x16x32_f16 v[76:79], v[44:47], v[136:139], v[76:79]
	v_mfma_f32_16x16x32_f16 v[72:75], v[60:63], v[136:139], v[72:75]
	s_waitcnt lgkmcnt(3)
	v_mfma_f32_16x16x32_f16 v[28:31], v[44:47], v[144:147], v[28:31]
	v_mfma_f32_16x16x32_f16 v[24:27], v[60:63], v[144:147], v[24:27]
	s_waitcnt lgkmcnt(1)
	v_mfma_f32_16x16x32_f16 v[12:15], v[44:47], v[152:155], v[12:15]
	v_mfma_f32_16x16x32_f16 v[8:11], v[60:63], v[152:155], v[8:11]
	v_mfma_f32_16x16x32_f16 v[92:95], v[56:59], v[96:99], v[92:95]
	v_mfma_f32_16x16x32_f16 v[88:91], v[64:67], v[96:99], v[88:91]
	v_mfma_f32_16x16x32_f16 v[76:79], v[56:59], v[140:143], v[76:79]
	v_mfma_f32_16x16x32_f16 v[72:75], v[64:67], v[140:143], v[72:75]
	v_mfma_f32_16x16x32_f16 v[28:31], v[56:59], v[148:151], v[28:31]
	v_mfma_f32_16x16x32_f16 v[24:27], v[64:67], v[148:151], v[24:27]
	s_waitcnt lgkmcnt(0)
	v_mfma_f32_16x16x32_f16 v[12:15], v[56:59], v[156:159], v[12:15]
	v_mfma_f32_16x16x32_f16 v[8:11], v[64:67], v[156:159], v[8:11]
	s_setprio 0
	s_barrier
	s_add_i32 s48, 0, 0x14000
	s_add_u32 s46, s46, s10
	s_addc_u32 s47, s47, s11
	s_mov_b32 m0, s61
	v_add_u32_e32 v64, s48, v128
	ds_read_b128 v[44:47], v64
	ds_read_b128 v[56:59], v64 offset:1024
	ds_read_b128 v[60:63], v64 offset:2048
	ds_read_b128 v[64:67], v64 offset:3072
	global_load_lds_dwordx4 v102, s[46:47]
	s_mov_b32 m0, s62
	s_nop 0
	global_load_lds_dwordx4 v106, s[46:47]
	s_waitcnt vmcnt(6)
	s_barrier
	s_setprio 1
	s_waitcnt lgkmcnt(3)
	v_mfma_f32_16x16x32_f16 v[84:87], v[44:47], v[80:83], v[84:87]
	v_mfma_f32_16x16x32_f16 v[52:55], v[44:47], v[136:139], v[52:55]
	s_waitcnt lgkmcnt(1)
	v_mfma_f32_16x16x32_f16 v[48:51], v[60:63], v[136:139], v[48:51]
	v_mfma_f32_16x16x32_f16 v[20:23], v[44:47], v[144:147], v[20:23]
	v_mfma_f32_16x16x32_f16 v[16:19], v[60:63], v[144:147], v[16:19]
	v_mfma_f32_16x16x32_f16 v[4:7], v[44:47], v[152:155], v[4:7]
	v_mfma_f32_16x16x32_f16 v[0:3], v[60:63], v[152:155], v[0:3]
	v_mfma_f32_16x16x32_f16 v[84:87], v[56:59], v[96:99], v[84:87]
	v_mfma_f32_16x16x32_f16 v[68:71], v[60:63], v[80:83], v[68:71]
	v_mfma_f32_16x16x32_f16 v[52:55], v[56:59], v[140:143], v[52:55]
	s_waitcnt lgkmcnt(0)
	v_mfma_f32_16x16x32_f16 v[48:51], v[64:67], v[140:143], v[48:51]
	v_mfma_f32_16x16x32_f16 v[20:23], v[56:59], v[148:151], v[20:23]
	v_mfma_f32_16x16x32_f16 v[16:19], v[64:67], v[148:151], v[16:19]
	v_mfma_f32_16x16x32_f16 v[4:7], v[56:59], v[156:159], v[4:7]
	v_mfma_f32_16x16x32_f16 v[0:3], v[64:67], v[156:159], v[0:3]
	v_mfma_f32_16x16x32_f16 v[68:71], v[64:67], v[96:99], v[68:71]
	s_setprio 0
	s_barrier
	s_mov_b32 m0, s64
	ds_read_b128 v[44:47], v132
	ds_read_b128 v[56:59], v132 offset:1024
	ds_read_b128 v[60:63], v132 offset:2048
	ds_read_b128 v[64:67], v132 offset:3072
	ds_read_b128 v[80:83], v133
	ds_read_b128 v[96:99], v133 offset:1024
	ds_read_b128 v[136:139], v133 offset:2048
	ds_read_b128 v[140:143], v133 offset:3072
	ds_read_b128 v[144:147], v133 offset:4096
	ds_read_b128 v[148:151], v133 offset:5120
	ds_read_b128 v[152:155], v133 offset:6144
	ds_read_b128 v[156:159], v133 offset:7168
	global_load_lds_dwordx4 v100, s[82:83]
	s_mov_b32 m0, s65
	s_add_i32 s46, s76, s54
	global_load_lds_dwordx4 v104, s[82:83]
	s_mov_b32 m0, s46
	s_nop 0
	global_load_lds_dwordx4 v102, s[84:85]
	s_add_i32 m0, s46, 0x2000
	s_nop 0
	global_load_lds_dwordx4 v106, s[84:85]
	s_barrier
	s_setprio 1
	s_waitcnt lgkmcnt(7)
	v_mfma_f32_16x16x32_f16 v[92:95], v[44:47], v[80:83], v[92:95]
	v_mfma_f32_16x16x32_f16 v[88:91], v[60:63], v[80:83], v[88:91]
	s_waitcnt lgkmcnt(5)
	v_mfma_f32_16x16x32_f16 v[76:79], v[44:47], v[136:139], v[76:79]
	v_mfma_f32_16x16x32_f16 v[72:75], v[60:63], v[136:139], v[72:75]
	s_waitcnt lgkmcnt(3)
	v_mfma_f32_16x16x32_f16 v[28:31], v[44:47], v[144:147], v[28:31]
	v_mfma_f32_16x16x32_f16 v[24:27], v[60:63], v[144:147], v[24:27]
	s_waitcnt lgkmcnt(1)
	v_mfma_f32_16x16x32_f16 v[12:15], v[44:47], v[152:155], v[12:15]
	v_mfma_f32_16x16x32_f16 v[8:11], v[60:63], v[152:155], v[8:11]
	v_mfma_f32_16x16x32_f16 v[92:95], v[56:59], v[96:99], v[92:95]
	v_mfma_f32_16x16x32_f16 v[88:91], v[64:67], v[96:99], v[88:91]
	v_mfma_f32_16x16x32_f16 v[76:79], v[56:59], v[140:143], v[76:79]
	v_mfma_f32_16x16x32_f16 v[72:75], v[64:67], v[140:143], v[72:75]
	v_mfma_f32_16x16x32_f16 v[28:31], v[56:59], v[148:151], v[28:31]
	v_mfma_f32_16x16x32_f16 v[24:27], v[64:67], v[148:151], v[24:27]
	s_waitcnt lgkmcnt(0)
	v_mfma_f32_16x16x32_f16 v[12:15], v[56:59], v[156:159], v[12:15]
	v_mfma_f32_16x16x32_f16 v[8:11], v[64:67], v[156:159], v[8:11]
	s_setprio 0
	s_barrier
	s_add_i32 s46, s48, s54
	s_mov_b32 m0, s46
	ds_read_b128 v[44:47], v134
	ds_read_b128 v[56:59], v134 offset:1024
	ds_read_b128 v[60:63], v134 offset:2048
	ds_read_b128 v[64:67], v134 offset:3072
	global_load_lds_dwordx4 v102, s[86:87]
	s_add_i32 m0, s46, 0x2000
	s_nop 0
	global_load_lds_dwordx4 v106, s[86:87]
	s_waitcnt vmcnt(6)
	s_barrier
	s_setprio 1
	s_waitcnt lgkmcnt(3)
	v_mfma_f32_16x16x32_f16 v[84:87], v[44:47], v[80:83], v[84:87]
	s_waitcnt lgkmcnt(1)
	v_mfma_f32_16x16x32_f16 v[68:71], v[60:63], v[80:83], v[68:71]
	v_mfma_f32_16x16x32_f16 v[52:55], v[44:47], v[136:139], v[52:55]
	v_mfma_f32_16x16x32_f16 v[48:51], v[60:63], v[136:139], v[48:51]
	v_mfma_f32_16x16x32_f16 v[20:23], v[44:47], v[144:147], v[20:23]
	v_mfma_f32_16x16x32_f16 v[16:19], v[60:63], v[144:147], v[16:19]
	v_mfma_f32_16x16x32_f16 v[4:7], v[44:47], v[152:155], v[4:7]
	v_mfma_f32_16x16x32_f16 v[0:3], v[60:63], v[152:155], v[0:3]
	v_mfma_f32_16x16x32_f16 v[84:87], v[56:59], v[96:99], v[84:87]
	s_waitcnt lgkmcnt(0)
	v_mfma_f32_16x16x32_f16 v[80:83], v[64:67], v[96:99], v[68:71]
	v_mfma_f32_16x16x32_f16 v[52:55], v[56:59], v[140:143], v[52:55]
	v_mfma_f32_16x16x32_f16 v[48:51], v[64:67], v[140:143], v[48:51]
	v_mfma_f32_16x16x32_f16 v[20:23], v[56:59], v[148:151], v[20:23]
	v_mfma_f32_16x16x32_f16 v[16:19], v[64:67], v[148:151], v[16:19]
	v_mfma_f32_16x16x32_f16 v[4:7], v[56:59], v[156:159], v[4:7]
	v_mfma_f32_16x16x32_f16 v[0:3], v[64:67], v[156:159], v[0:3]
	s_setprio 0
	s_add_i32 s75, s75, 3
	s_add_u32 s44, s44, 0x180
	s_addc_u32 s45, s45, 0
	s_cmp_ge_i32 s75, s66
	s_cbranch_scc1 .Lrot_exit_mlp1
	s_add_u32 s78, s40, s44
	s_addc_u32 s79, s41, s45
	s_add_u32 s80, s42, s44
	s_addc_u32 s81, s43, s45
	s_add_u32 s46, s40, s44
	s_addc_u32 s47, s41, s45
	s_add_u32 s46, s46, 0x180
	s_addc_u32 s47, s47, 0
	s_add_u32 s48, s42, s44
	s_addc_u32 s49, s43, s45
	s_add_u32 s76, s48, 0x180
	s_addc_u32 s77, s49, 0
	s_cmp_eq_u32 s67, s75
	s_cselect_b32 s49, s7, s47
	s_cselect_b32 s48, s6, s46
	s_cselect_b32 s47, s5, s77
	s_cselect_b32 s46, s4, s76
	s_add_u32 s82, s48, 0x80
	s_addc_u32 s83, s49, 0
	s_add_u32 s84, s46, 0x80
	s_addc_u32 s85, s47, 0
	s_add_u32 s86, s84, s10
	s_addc_u32 s87, s85, s11
	s_add_i32 s76, s19, s54
	s_barrier
	s_branch .LBB5_55

	.amdhsa_kernel _Z9k_gemm128IN4g1289EpiGeluLNEEvNS0_4GemmET_
		.amdhsa_group_segment_fixed_size 0
		.amdhsa_private_segment_fixed_size 0
		.amdhsa_kernarg_size 344
		.amdhsa_user_sgpr_count 2
		.amdhsa_user_sgpr_dispatch_ptr 0
		.amdhsa_user_sgpr_queue_ptr 0
		.amdhsa_user_sgpr_kernarg_segment_ptr 1
		.amdhsa_user_sgpr_dispatch_id 0
		.amdhsa_user_sgpr_kernarg_preload_length 0
		.amdhsa_user_sgpr_kernarg_preload_offset 0
		.amdhsa_user_sgpr_private_segment_size 0
		.amdhsa_uses_dynamic_stack 0
		.amdhsa_enable_private_segment 0
		.amdhsa_system_sgpr_workgroup_id_x 1
		.amdhsa_system_sgpr_workgroup_id_y 0
		.amdhsa_system_sgpr_workgroup_id_z 0
		.amdhsa_system_sgpr_workgroup_info 0
		.amdhsa_system_vgpr_workitem_id 0
		.amdhsa_next_free_vgpr 170
		.amdhsa_next_free_sgpr 88
		.amdhsa_accum_offset 172
		.amdhsa_reserve_vcc 1
		.amdhsa_float_round_mode_32 0
		.amdhsa_float_round_mode_16_64 0
		.amdhsa_float_denorm_mode_32 3
		.amdhsa_float_denorm_mode_16_64 3
		.amdhsa_dx10_clamp 1
		.amdhsa_ieee_mode 1
		.amdhsa_fp16_overflow 0
		.amdhsa_tg_split 0
		.amdhsa_exception_fp_ieee_invalid_op 0
		.amdhsa_exception_fp_denorm_src 0
		.amdhsa_exception_fp_ieee_div_zero 0
		.amdhsa_exception_fp_ieee_overflow 0
		.amdhsa_exception_fp_ieee_underflow 0
		.amdhsa_exception_fp_ieee_inexact 0
		.amdhsa_exception_int_div_zero 0
	.end_amdhsa_kernel
